# v26 + attention unit: the sink-logit load is issued with the unit's Q loads (covered by the existing pre-barrier wait) instead of after the barrier in front of the first MFMA
# speedup vs baseline: 1.0101x; 1.0017x over previous
; #define LAS __attribute__((address_space(3)))
; __device__ __forceinline__ void attn_phase(LAS unsigned char* lds, const bf16* U, bf16* YA, const float* sinks, const float* rel_bias, int G, int c, int wbase, int y8) {
;     ...
;         for (int kg = 0; kg < 4; ++kg) { const int key = 64 * kg + lane; int t = tok0 + key; if (t < b * SEQ) t = b * SEQ;
;             __builtin_amdgcn_global_load_lds((const unsigned*)(U + (size_t)t * NIN + C_K + kvh * 64 + 8 * wid), (LAS unsigned*)(lds + KIMG + wid * 4096 + kg * 1024), 16, 0, 0); }
; #pragma unroll
;         for (int j = 0; j < 4; ++j) { const int kg16 = 4 * (wid & 3) + j, key = 16 * kg16 + (lane >> 2); int t = tok0 + key; if (t < b * SEQ) t = b * SEQ;
;             __builtin_amdgcn_global_load_lds((const unsigned*)(U + (size_t)t * NIN + C_V + kvh * 64 + 32 * (wid >> 2) + 8 * (lane & 3)), (LAS unsigned*)(lds + VIMG + (wid >> 2) * 16384 + kg16 * 1024), 16, 0, 0); }
;         const size_t mq0 = (size_t)b * SEQ + n * 128 + 64 * qh;
;         bf16x8 qf[2][4];
; #pragma unroll
;         for (int qt = 0; qt < 2; ++qt)
; #pragma unroll
;             for (int d0 = 0; d0 < 4; ++d0) qf[qt][d0] = *(const bf16x8*)(U + (mq0 + 32 * qt + r32) * NIN + (kvh * 4 + g) * 64 + 16 * d0 + 8 * hi);
;         asm volatile("s_waitcnt vmcnt(0)" ::: "memory"); __syncthreads();
;         const float sink2 = sinks[kvh * 4 + g] * LOG2E; const LAS float* bt = rbt + g * 192 + 31 - r32 + 4 * hi;
; #pragma unroll
;         for (int qt = 0; qt < 2; ++qt) {
;             const int iq0 = 64 * qh + 32 * qt, kt0 = iq0 >> 5; const size_t mq = mq0 + 32 * qt;
;             f32x16 p[5];
; #pragma unroll
;             for (int jt = 0; jt < 5; ++jt) { f32x16 a = {};
; #pragma unroll
;                 for (int d0 = 0; d0 < 4; ++d0) { const bf16x8 kf = *(const LAS bf16x8*)(lds + KIMG + (2 * d0 + hi) * 4096 + (32 * (kt0 + jt) + r32) * 16); a = __builtin_amdgcn_mfma_f32_32x32x16_bf16(kf, qf[qt][d0], a, 0, 0, 0); }
.LBB0_554:
	s_or_b64 exec, exec, s[4:5]
	s_bfe_u32 s31, s33, 0x50002
	s_ashr_i32 s4, s33, 7
	s_lshl_b32 s5, s4, 12
	s_lshl_b32 s8, s31, 7
	s_or_b32 s6, s5, s8
	s_add_i32 s9, s6, 0xffffff80
	v_or_b32_e32 v4, s9, v113
	v_max_i32_e32 v2, s5, v4
	v_mov_b64_e32 v[0:1], s[10:11]
	v_mad_i64_i32 v[2:3], s[6:7], v2, s87, v[0:1]
	s_lshl_b32 s6, s84, 7
	s_mov_b32 s7, s40
	v_lshl_add_u64 v[2:3], v[2:3], 0, s[6:7]
	v_lshl_add_u64 v[2:3], v[2:3], 0, s[24:25]
	s_mov_b64 s[34:35], 0x800
	v_lshl_add_u64 v[2:3], v[2:3], 0, s[34:35]
	s_mov_b32 m0, s42
	v_mov_b32_e32 v8, 0x2c00
	global_load_lds_dwordx4 v[2:3], off
	v_or_b32_e32 v2, 64, v4
	v_max_i32_e32 v2, s5, v2
	v_mad_i64_i32 v[2:3], s[28:29], v2, s87, v[0:1]
	v_lshl_add_u64 v[2:3], v[2:3], 0, s[6:7]
	v_lshl_add_u64 v[2:3], v[2:3], 0, s[24:25]
	v_lshl_add_u64 v[2:3], v[2:3], 0, s[34:35]
	s_add_i32 m0, s42, 0x400
	v_add_u32_e32 v155, s77, v123
	global_load_lds_dwordx4 v[2:3], off
	v_add_u32_e32 v2, 0x80, v4
	v_max_i32_e32 v2, s5, v2
	v_mad_i64_i32 v[2:3], s[28:29], v2, s87, v[0:1]
	v_lshl_add_u64 v[2:3], v[2:3], 0, s[6:7]
	v_lshl_add_u64 v[2:3], v[2:3], 0, s[24:25]
	v_lshl_add_u64 v[2:3], v[2:3], 0, s[34:35]
	s_add_i32 m0, s42, 0x800
	v_add_u32_e32 v152, s59, v123
	global_load_lds_dwordx4 v[2:3], off
	v_add_u32_e32 v2, 0xc0, v4
	v_max_i32_e32 v2, s5, v2
	v_mad_i64_i32 v[2:3], s[28:29], v2, s87, v[0:1]
	v_lshl_add_u64 v[2:3], v[2:3], 0, s[6:7]
	v_lshl_add_u64 v[2:3], v[2:3], 0, s[24:25]
	v_lshl_add_u64 v[2:3], v[2:3], 0, s[34:35]
	s_add_i32 m0, s42, 0xc00
	v_or_b32_e32 v4, s9, v119
	global_load_lds_dwordx4 v[2:3], off
	v_add_u32_e32 v2, s44, v4
	v_max_i32_e32 v2, s5, v2
	v_mad_i64_i32 v[2:3], s[28:29], v2, s87, v[0:1]
	v_lshl_add_u64 v[2:3], v[2:3], 0, s[6:7]
	v_lshl_add_u64 v[2:3], v[2:3], 0, s[26:27]
	v_lshl_add_u64 v[2:3], v[2:3], 0, v[232:233]
	s_mov_b64 s[34:35], 0xa00
	v_lshl_add_u64 v[2:3], v[2:3], 0, s[34:35]
	s_mov_b32 m0, s85
	v_add_u32_e32 v153, s65, v123
	global_load_lds_dwordx4 v[2:3], off
	v_add_u32_e32 v2, s45, v4
	v_max_i32_e32 v2, s5, v2
	v_mad_i64_i32 v[2:3], s[28:29], v2, s87, v[0:1]
	v_lshl_add_u64 v[2:3], v[2:3], 0, s[6:7]
	v_lshl_add_u64 v[2:3], v[2:3], 0, s[26:27]
	v_lshl_add_u64 v[2:3], v[2:3], 0, v[232:233]
	v_lshl_add_u64 v[2:3], v[2:3], 0, s[34:35]
	s_mov_b32 m0, s48
	v_add_u32_e32 v154, s76, v123
	global_load_lds_dwordx4 v[2:3], off
	v_add_u32_e32 v2, s52, v4
	v_max_i32_e32 v2, s5, v2
	v_mad_i64_i32 v[2:3], s[28:29], v2, s87, v[0:1]
	v_lshl_add_u64 v[2:3], v[2:3], 0, s[6:7]
	v_lshl_add_u64 v[2:3], v[2:3], 0, s[26:27]
	v_lshl_add_u64 v[2:3], v[2:3], 0, v[232:233]
	v_lshl_add_u64 v[2:3], v[2:3], 0, s[34:35]
	s_mov_b32 m0, s46
	s_nop 0
	global_load_lds_dwordx4 v[2:3], off
	v_add_u32_e32 v2, s53, v4
	v_max_i32_e32 v2, s5, v2
	s_ashr_i32 s5, s4, 31
	v_mad_i64_i32 v[0:1], s[28:29], v2, s87, v[0:1]
	s_lshl_b64 s[4:5], s[4:5], 12
	v_lshl_add_u64 v[0:1], v[0:1], 0, s[6:7]
	s_or_b32 s4, s4, s8
	v_lshl_add_u64 v[0:1], v[0:1], 0, s[26:27]
	s_or_b64 s[28:29], s[4:5], s[16:17]
	s_lshl_b32 s4, s84, 8
	v_lshl_add_u64 v[0:1], v[0:1], 0, v[232:233]
	s_add_i32 s6, s4, s43
	v_lshl_add_u64 v[0:1], v[0:1], 0, s[34:35]
	s_mov_b32 m0, s47
	s_ashr_i32 s7, s6, 31
	global_load_lds_dwordx4 v[0:1], off
	v_lshl_add_u64 v[4:5], s[6:7], 1, v[110:111]
	v_or_b32_e32 v0, s28, v108
	v_mad_u64_u32 v[6:7], s[6:7], v0, s87, v[4:5]
	v_mad_i32_i24 v7, s5, v8, v7
	global_load_dwordx4 v[0:3], v[6:7], off
	global_load_dwordx4 v[96:99], v[6:7], off offset:32
	global_load_dwordx4 v[100:103], v[6:7], off offset:64
	global_load_dwordx4 v[104:107], v[6:7], off offset:96
	v_or_b32_e32 v6, s28, v118
	s_add_i32 s8, s30, s41
	v_mad_u64_u32 v[4:5], s[6:7], v6, s87, v[4:5]
	s_ashr_i32 s9, s8, 31
	v_mad_i32_i24 v5, s5, v8, v5
	s_lshl_b64 s[4:5], s[8:9], 2
	s_add_u32 s4, s36, s4
	s_addc_u32 s5, s37, s5
	global_load_dword v180, v233, s[4:5]
	global_load_dwordx4 v[92:95], v[4:5], off
	global_load_dwordx4 v[88:91], v[4:5], off offset:32
	global_load_dwordx4 v[84:87], v[4:5], off offset:64
	global_load_dwordx4 v[80:83], v[4:5], off offset:96
	s_waitcnt vmcnt(0)
	s_waitcnt vmcnt(0) lgkmcnt(0)
	s_barrier
	v_mov_b32_e32 v4, v180
	v_add_u32_e32 v8, s58, v123
	s_cmp_eq_u32 s31, 0
	s_cselect_b64 s[4:5], -1, 0
	s_and_b64 s[6:7], s[4:5], s[20:21]
	ds_read_b128 v[156:159], v155 offset:8192
	s_waitcnt vmcnt(0)
	v_mul_f32_e32 v151, 0x3fb8aa3b, v4
	ds_read_b128 v[4:7], v8
	s_waitcnt lgkmcnt(0)
	v_mfma_f32_32x32x16_bf16 v[64:79], v[4:7], v[0:3], 0
	ds_read_b128 v[4:7], v8 offset:8192
	s_waitcnt lgkmcnt(0)
	v_mfma_f32_32x32x16_bf16 v[64:79], v[4:7], v[96:99], v[64:79]
	ds_read_b128 v[4:7], v8 offset:16384
	s_waitcnt lgkmcnt(0)
	v_mfma_f32_32x32x16_bf16 v[64:79], v[4:7], v[100:103], v[64:79]
	ds_read_b128 v[4:7], v8 offset:24576
	s_waitcnt lgkmcnt(0)
	v_mfma_f32_32x32x16_bf16 v[64:79], v[4:7], v[104:107], v[64:79]
	ds_read_b128 v[4:7], v152
	s_waitcnt lgkmcnt(0)
	v_mfma_f32_32x32x16_bf16 v[48:63], v[4:7], v[0:3], 0
	ds_read_b128 v[4:7], v152 offset:8192
	s_waitcnt lgkmcnt(0)
	v_mfma_f32_32x32x16_bf16 v[48:63], v[4:7], v[96:99], v[48:63]
	ds_read_b128 v[4:7], v152 offset:16384
	s_waitcnt lgkmcnt(0)
	v_mfma_f32_32x32x16_bf16 v[48:63], v[4:7], v[100:103], v[48:63]
	ds_read_b128 v[4:7], v152 offset:24576
	s_waitcnt lgkmcnt(0)
	v_mfma_f32_32x32x16_bf16 v[48:63], v[4:7], v[104:107], v[48:63]
	ds_read_b128 v[4:7], v153
	s_waitcnt lgkmcnt(0)
	v_mfma_f32_32x32x16_bf16 v[32:47], v[4:7], v[0:3], 0
	ds_read_b128 v[4:7], v153 offset:8192
	s_waitcnt lgkmcnt(0)
	v_mfma_f32_32x32x16_bf16 v[32:47], v[4:7], v[96:99], v[32:47]
	ds_read_b128 v[4:7], v153 offset:16384
	s_waitcnt lgkmcnt(0)
	v_mfma_f32_32x32x16_bf16 v[32:47], v[4:7], v[100:103], v[32:47]
	ds_read_b128 v[4:7], v153 offset:24576
	s_waitcnt lgkmcnt(0)
; #define LAS __attribute__((address_space(3)))
; __device__ __forceinline__ int crow(int r, int hi) { return (r & 3) + 8 * (r >> 2) + 4 * hi; }
; __device__ __forceinline__ int crow(int r, int hi) { return (r & 3) + 8 * (r >> 2) + 4 * hi; }
; __device__ __forceinline__ void attn_phase(LAS unsigned char* lds, const bf16* U, bf16* YA, const float* sinks, const float* rel_bias, int G, int c, int wbase, int y8) {
;     ...
;             for (int jt = 0; jt < 5; ++jt) { f32x16 a = {};
; #pragma unroll
;                 for (int d0 = 0; d0 < 4; ++d0) { const bf16x8 kf = *(const LAS bf16x8*)(lds + KIMG + (2 * d0 + hi) * 4096 + (32 * (kt0 + jt) + r32) * 16); a = __builtin_amdgcn_mfma_f32_32x32x16_bf16(kf, qf[qt][d0], a, 0, 0, 0); }
;                 p[jt] = a; }
;             float mx = sink2;
; #pragma unroll
;             for (int jt = 0; jt < 5; ++jt)
; #pragma unroll
;                 for (int r = 0; r < 16; ++r) { float s = p[jt][r] + bt[32 * jt + (r & 3) + 8 * (r >> 2)];
;                     if (n == 0) { if (32 * (kt0 + jt) + crow(r, hi) < 128) s = -1.0e30f; }
;                     p[jt][r] = s; mx = fmaxf(mx, s); }
	v_mfma_f32_32x32x16_bf16 v[32:47], v[4:7], v[104:107], v[32:47]
	ds_read_b128 v[4:7], v154
	s_waitcnt lgkmcnt(0)
	v_mfma_f32_32x32x16_bf16 v[16:31], v[4:7], v[0:3], 0
	ds_read_b128 v[4:7], v154 offset:8192
	s_waitcnt lgkmcnt(0)
	v_mfma_f32_32x32x16_bf16 v[16:31], v[4:7], v[96:99], v[16:31]
	ds_read_b128 v[4:7], v154 offset:16384
	s_waitcnt lgkmcnt(0)
	v_mfma_f32_32x32x16_bf16 v[16:31], v[4:7], v[100:103], v[16:31]
	ds_read_b128 v[4:7], v154 offset:24576
	s_waitcnt lgkmcnt(0)
	v_mfma_f32_32x32x16_bf16 v[16:31], v[4:7], v[104:107], v[16:31]
	ds_read_b128 v[4:7], v155
	s_waitcnt lgkmcnt(0)
	v_mfma_f32_32x32x16_bf16 v[0:15], v[4:7], v[0:3], 0
	v_mfma_f32_32x32x16_bf16 v[0:15], v[156:159], v[96:99], v[0:15]
	ds_read_b128 v[96:99], v155 offset:16384
	s_waitcnt lgkmcnt(0)
	v_mfma_f32_32x32x16_bf16 v[0:15], v[96:99], v[100:103], v[0:15]
	ds_read_b128 v[96:99], v155 offset:24576
	v_mov_b32_e32 v102, 0xf149f2ca
	s_waitcnt lgkmcnt(0)
	v_mfma_f32_32x32x16_bf16 v[0:15], v[96:99], v[104:107], v[0:15]
	ds_read2_b32 v[96:97], v121 offset0:31 offset1:32
	ds_read2_b32 v[98:99], v121 offset0:33 offset1:34
	s_waitcnt lgkmcnt(1)
	v_add_f32_e32 v64, v64, v96
	v_cndmask_b32_e64 v96, v64, v102, s[4:5]
	v_add_f32_e32 v64, v65, v97
	s_waitcnt lgkmcnt(0)
	v_add_f32_e32 v65, v66, v98
	v_cndmask_b32_e64 v66, v65, v102, s[4:5]
	v_add_f32_e32 v65, v67, v99
	ds_read2_b32 v[98:99], v121 offset0:39 offset1:40
	v_cndmask_b32_e64 v64, v64, v102, s[4:5]
	v_max3_f32 v97, v151, v96, v64
	v_cndmask_b32_e64 v65, v65, v102, s[4:5]
	v_max3_f32 v97, v97, v66, v65
	s_waitcnt lgkmcnt(0)
	v_add_f32_e32 v67, v68, v98
	v_cndmask_b32_e64 v68, v67, v102, s[4:5]
	v_add_f32_e32 v67, v69, v99
	ds_read2_b32 v[98:99], v121 offset0:41 offset1:42
	v_cndmask_b32_e64 v67, v67, v102, s[4:5]
	v_max3_f32 v69, v97, v68, v67
	s_waitcnt lgkmcnt(0)
	v_add_f32_e32 v70, v70, v98
	v_cndmask_b32_e64 v97, v70, v102, s[4:5]
	v_add_f32_e32 v70, v71, v99
	ds_read2_b32 v[98:99], v121 offset0:47 offset1:48
	v_cndmask_b32_e64 v70, v70, v102, s[4:5]
	v_max3_f32 v100, v69, v97, v70
	s_waitcnt lgkmcnt(0)
	v_add_f32_e32 v69, v72, v98
	v_cndmask_b32_e64 v71, v69, v102, s[4:5]
	v_add_f32_e32 v69, v73, v99
	ds_read2_b32 v[98:99], v121 offset0:49 offset1:50
	v_cndmask_b32_e64 v69, v69, v102, s[4:5]
	v_max3_f32 v100, v100, v71, v69
	s_waitcnt lgkmcnt(0)
	v_add_f32_e32 v72, v74, v98
	v_cndmask_b32_e64 v73, v72, v102, s[4:5]
	v_add_f32_e32 v72, v75, v99
	ds_read2_b32 v[98:99], v121 offset0:55 offset1:56
	v_cndmask_b32_e64 v72, v72, v102, s[4:5]
	v_max3_f32 v100, v100, v73, v72
	s_waitcnt lgkmcnt(0)
	v_add_f32_e32 v74, v76, v98
	v_cndmask_b32_e64 v75, v74, v102, s[4:5]
	v_add_f32_e32 v74, v77, v99
	ds_read2_b32 v[76:77], v121 offset0:57 offset1:58
	v_cndmask_b32_e64 v74, v74, v102, s[4:5]
	v_max3_f32 v98, v100, v75, v74
	s_waitcnt lgkmcnt(0)
	v_add_f32_e32 v76, v78, v76
	v_cndmask_b32_e64 v78, v76, v102, s[4:5]
	v_add_f32_e32 v76, v79, v77
	v_cndmask_b32_e64 v76, v76, v102, s[4:5]
	v_max3_f32 v79, v98, v78, v76
	ds_read2_b32 v[98:99], v121 offset0:63 offset1:64
	s_waitcnt lgkmcnt(0)
	v_add_f32_e32 v48, v48, v98
	v_cndmask_b32_e64 v77, v48, v102, s[4:5]
	v_add_f32_e32 v48, v49, v99
	ds_read2_b32 v[98:99], v121 offset0:65 offset1:66
	v_cndmask_b32_e64 v48, v48, v102, s[4:5]
	v_max3_f32 v79, v79, v77, v48
	s_waitcnt lgkmcnt(0)
	v_add_f32_e32 v49, v50, v98
	v_cndmask_b32_e64 v50, v49, v102, s[4:5]
	v_add_f32_e32 v49, v51, v99
	ds_read2_b32 v[98:99], v121 offset0:71 offset1:72
	v_cndmask_b32_e64 v49, v49, v102, s[4:5]
	v_max3_f32 v79, v79, v50, v49
	s_waitcnt lgkmcnt(0)
	v_add_f32_e32 v51, v52, v98
	v_cndmask_b32_e64 v52, v51, v102, s[4:5]
	v_add_f32_e32 v51, v53, v99
	ds_read2_b32 v[98:99], v121 offset0:73 offset1:74
	v_cndmask_b32_e64 v51, v51, v102, s[4:5]
	v_max3_f32 v53, v79, v52, v51
	s_waitcnt lgkmcnt(0)
	v_add_f32_e32 v54, v54, v98
	v_cndmask_b32_e64 v79, v54, v102, s[4:5]
	v_add_f32_e32 v54, v55, v99
	ds_read2_b32 v[98:99], v121 offset0:79 offset1:80
	v_cndmask_b32_e64 v54, v54, v102, s[4:5]
	v_max3_f32 v100, v53, v79, v54
	s_waitcnt lgkmcnt(0)
	v_add_f32_e32 v53, v56, v98
	v_cndmask_b32_e64 v55, v53, v102, s[4:5]
	v_add_f32_e32 v53, v57, v99
	ds_read2_b32 v[98:99], v121 offset0:81 offset1:82
	v_cndmask_b32_e64 v53, v53, v102, s[4:5]
	v_max3_f32 v100, v100, v55, v53
	s_waitcnt lgkmcnt(0)
	v_add_f32_e32 v56, v58, v98
	v_cndmask_b32_e64 v57, v56, v102, s[4:5]
	v_add_f32_e32 v56, v59, v99
	ds_read2_b32 v[98:99], v121 offset0:87 offset1:88
	v_cndmask_b32_e64 v56, v56, v102, s[4:5]
	v_max3_f32 v100, v100, v57, v56
	s_waitcnt lgkmcnt(0)
	v_add_f32_e32 v58, v60, v98
	v_cndmask_b32_e64 v59, v58, v102, s[4:5]
	v_add_f32_e32 v58, v61, v99
	ds_read2_b32 v[60:61], v121 offset0:89 offset1:90
	v_cndmask_b32_e64 v58, v58, v102, s[4:5]
	v_max3_f32 v98, v100, v59, v58
	ds_read2_b32 v[100:101], v121 offset0:111 offset1:112
	s_waitcnt lgkmcnt(1)
	v_add_f32_e32 v60, v62, v60
	v_cndmask_b32_e64 v62, v60, v102, s[4:5]
	v_add_f32_e32 v60, v63, v61
	v_cndmask_b32_e64 v60, v60, v102, s[4:5]
	v_max3_f32 v63, v98, v62, v60
	ds_read2_b32 v[98:99], v121 offset0:95 offset1:96
	s_waitcnt lgkmcnt(0)
	v_add_f32_e32 v32, v32, v98
	v_cndmask_b32_e64 v61, v32, v102, s[6:7]
	v_add_f32_e32 v32, v33, v99
	ds_read2_b32 v[98:99], v121 offset0:97 offset1:98
	v_cndmask_b32_e64 v33, v32, v102, s[6:7]
	v_max3_f32 v32, v63, v61, v33
	s_waitcnt lgkmcnt(0)
	v_add_f32_e32 v34, v34, v98
	v_cndmask_b32_e64 v63, v34, v102, s[6:7]
	v_add_f32_e32 v34, v35, v99
	ds_read2_b32 v[98:99], v121 offset0:103 offset1:104
	v_cndmask_b32_e64 v34, v34, v102, s[6:7]
	v_max3_f32 v32, v32, v63, v34
	s_waitcnt lgkmcnt(0)
; __device__ __forceinline__ int crow(int r, int hi) { return (r & 3) + 8 * (r >> 2) + 4 * hi; }
; __device__ __forceinline__ int crow(int r, int hi) { return (r & 3) + 8 * (r >> 2) + 4 * hi; }
; __device__ __forceinline__ void attn_phase(LAS unsigned char* lds, const bf16* U, bf16* YA, const float* sinks, const float* rel_bias, int G, int c, int wbase, int y8) {
;     ...
;             float mx = sink2;
; #pragma unroll
;             for (int jt = 0; jt < 5; ++jt)
; #pragma unroll
;                 for (int r = 0; r < 16; ++r) { float s = p[jt][r] + bt[32 * jt + (r & 3) + 8 * (r >> 2)];
;                     if (n == 0) { if (32 * (kt0 + jt) + crow(r, hi) < 128) s = -1.0e30f; }
;                     p[jt][r] = s; mx = fmaxf(mx, s); }
	v_add_f32_e32 v35, v36, v98
	v_cndmask_b32_e64 v36, v35, v102, s[6:7]
	v_add_f32_e32 v35, v37, v99
	ds_read2_b32 v[98:99], v121 offset0:105 offset1:106
	v_cndmask_b32_e64 v35, v35, v102, s[6:7]
	v_max3_f32 v32, v32, v36, v35
	s_waitcnt lgkmcnt(0)
	v_add_f32_e32 v37, v38, v98
	v_cndmask_b32_e64 v98, v37, v102, s[6:7]
	v_add_f32_e32 v37, v39, v99
	v_cndmask_b32_e64 v38, v37, v102, s[6:7]
	v_add_f32_e32 v37, v40, v100
	v_cndmask_b32_e64 v39, v37, v102, s[6:7]
	v_add_f32_e32 v37, v41, v101
	ds_read2_b32 v[100:101], v121 offset0:113 offset1:114
	v_max3_f32 v32, v32, v98, v38
	v_cndmask_b32_e64 v37, v37, v102, s[6:7]
	v_max3_f32 v32, v32, v39, v37
	s_waitcnt lgkmcnt(0)
	v_add_f32_e32 v40, v42, v100
	v_cndmask_b32_e64 v41, v40, v102, s[6:7]
	v_add_f32_e32 v40, v43, v101
	ds_read2_b32 v[100:101], v121 offset0:119 offset1:120
	v_cndmask_b32_e64 v40, v40, v102, s[6:7]
	v_max3_f32 v32, v32, v41, v40
	s_waitcnt lgkmcnt(0)
	v_add_f32_e32 v42, v44, v100
	v_cndmask_b32_e64 v43, v42, v102, s[6:7]
	v_add_f32_e32 v42, v45, v101
	ds_read2_b32 v[44:45], v121 offset0:121 offset1:122
	ds_read2_b32 v[100:101], v121 offset0:127 offset1:128
	v_cndmask_b32_e64 v42, v42, v102, s[6:7]
	v_max3_f32 v32, v32, v43, v42
	s_waitcnt lgkmcnt(1)
	v_add_f32_e32 v44, v46, v44
	s_waitcnt lgkmcnt(0)
	v_add_f32_e32 v16, v16, v100
	v_cndmask_b32_e64 v46, v44, v102, s[6:7]
	v_add_f32_e32 v44, v47, v45
	v_cndmask_b32_e64 v45, v16, v102, s[6:7]
	v_add_f32_e32 v16, v17, v101
	ds_read2_b32 v[100:101], v121 offset0:129 offset1:130
	v_cndmask_b32_e64 v44, v44, v102, s[6:7]
	v_max3_f32 v32, v32, v46, v44
	v_cndmask_b32_e64 v16, v16, v102, s[6:7]
	v_max3_f32 v32, v32, v45, v16
	s_waitcnt lgkmcnt(0)
	v_add_f32_e32 v17, v18, v100
	v_cndmask_b32_e64 v18, v17, v102, s[6:7]
	v_add_f32_e32 v17, v19, v101
	ds_read2_b32 v[100:101], v121 offset0:135 offset1:136
	v_cndmask_b32_e64 v17, v17, v102, s[6:7]
	v_max3_f32 v32, v32, v18, v17
	s_waitcnt lgkmcnt(0)
	v_add_f32_e32 v19, v20, v100
	v_cndmask_b32_e64 v20, v19, v102, s[6:7]
	v_add_f32_e32 v19, v21, v101
	ds_read2_b32 v[100:101], v121 offset0:137 offset1:138
	v_cndmask_b32_e64 v19, v19, v102, s[6:7]
	v_max3_f32 v32, v32, v20, v19
	s_waitcnt lgkmcnt(0)
	v_add_f32_e32 v21, v22, v100
	v_cndmask_b32_e64 v22, v21, v102, s[6:7]
	v_add_f32_e32 v21, v23, v101
	ds_read2_b32 v[100:101], v121 offset0:143 offset1:144
	v_cndmask_b32_e64 v21, v21, v102, s[6:7]
	v_max3_f32 v32, v32, v22, v21
	s_waitcnt lgkmcnt(0)
	v_add_f32_e32 v23, v24, v100
	v_cndmask_b32_e64 v24, v23, v102, s[6:7]
	v_add_f32_e32 v23, v25, v101
	ds_read2_b32 v[100:101], v121 offset0:145 offset1:146
	v_cndmask_b32_e64 v23, v23, v102, s[6:7]
	v_max3_f32 v32, v32, v24, v23
	s_waitcnt lgkmcnt(0)
	v_add_f32_e32 v25, v26, v100
	v_cndmask_b32_e64 v26, v25, v102, s[6:7]
	v_add_f32_e32 v25, v27, v101
	ds_read2_b32 v[100:101], v121 offset0:151 offset1:152
	v_cndmask_b32_e64 v25, v25, v102, s[6:7]
	v_max3_f32 v32, v32, v26, v25
	s_waitcnt lgkmcnt(0)
	v_add_f32_e32 v27, v28, v100
	v_cndmask_b32_e64 v28, v27, v102, s[6:7]
	v_add_f32_e32 v27, v29, v101
	ds_read2_b32 v[100:101], v121 offset0:153 offset1:154
	v_cndmask_b32_e64 v27, v27, v102, s[6:7]
	v_max3_f32 v32, v32, v28, v27
	s_waitcnt lgkmcnt(0)
	v_add_f32_e32 v29, v30, v100
	v_cndmask_b32_e64 v30, v29, v102, s[6:7]
	v_add_f32_e32 v29, v31, v101
	ds_read2_b32 v[100:101], v121 offset0:159 offset1:160
	v_cndmask_b32_e64 v29, v29, v102, s[6:7]
	v_max3_f32 v32, v32, v30, v29
	s_waitcnt lgkmcnt(0)
	v_add_f32_e32 v47, v0, v100
	v_add_f32_e32 v31, v1, v101
	ds_read2_b32 v[0:1], v121 offset0:161 offset1:162
	v_max3_f32 v32, v32, v47, v31
	s_waitcnt lgkmcnt(0)
	v_add_f32_e32 v172, v2, v0
	v_add_f32_e32 v171, v3, v1
	ds_read2_b32 v[0:1], v121 offset0:167 offset1:168
	v_max3_f32 v2, v32, v172, v171
	s_waitcnt lgkmcnt(0)
	v_add_f32_e32 v174, v4, v0
	v_add_f32_e32 v173, v5, v1
	ds_read2_b32 v[0:1], v121 offset0:169 offset1:170
	v_max3_f32 v2, v2, v174, v173
	s_waitcnt lgkmcnt(0)
	v_add_f32_e32 v176, v6, v0
	v_add_f32_e32 v175, v7, v1
	ds_read2_b32 v[0:1], v121 offset0:175 offset1:176
	v_max3_f32 v2, v2, v176, v175
	s_waitcnt lgkmcnt(0)
	v_add_f32_e32 v177, v8, v0
	v_add_f32_e32 v8, v9, v1
	ds_read2_b32 v[0:1], v121 offset0:177 offset1:178
	v_max3_f32 v2, v2, v177, v8
	s_waitcnt lgkmcnt(0)
	v_add_f32_e32 v10, v10, v0
	v_add_f32_e32 v9, v11, v1
	ds_read2_b32 v[0:1], v121 offset0:183 offset1:184
	v_max3_f32 v2, v2, v10, v9
	s_waitcnt lgkmcnt(0)
	v_add_f32_e32 v12, v12, v0
	v_add_f32_e32 v11, v13, v1
	ds_read2_b32 v[0:1], v121 offset0:185 offset1:186
	v_max3_f32 v2, v2, v12, v11
	s_waitcnt lgkmcnt(0)
; #define LAS __attribute__((address_space(3)))
; __device__ __forceinline__ float sum_x32(float v) { const unsigned u = __builtin_bit_cast(unsigned, v); auto rr = __builtin_amdgcn_permlane32_swap(u, u, false, false); return __builtin_bit_cast(float, (unsigned)rr[0]) + __builtin_bit_cast(float, (unsigned)rr[1]); }
; __device__ __forceinline__ float max_x32(float v) { const unsigned u = __builtin_bit_cast(unsigned, v); auto rr = __builtin_amdgcn_permlane32_swap(u, u, false, false); return fmaxf(__builtin_bit_cast(float, (unsigned)rr[0]), __builtin_bit_cast(float, (unsigned)rr[1])); }
; __device__ __forceinline__ unsigned cvt_pk_bf16(float lo, float hi) { unsigned r; asm volatile("v_cvt_pk_bf16_f32 %0, %1, %2" : "=v"(r) : "v"(lo), "v"(hi)); return r; }
; __device__ __forceinline__ void attn_phase(LAS unsigned char* lds, const bf16* U, bf16* YA, const float* sinks, const float* rel_bias, int G, int c, int wbase, int y8) {
;     ...
;             mx = max_x32(mx);
;             float l = 0.f;
; #pragma unroll
;             for (int jt = 0; jt < 5; ++jt)
; #pragma unroll
;                 for (int r = 0; r < 16; ++r) { const float e = __builtin_amdgcn_exp2f(p[jt][r] - mx); p[jt][r] = e; l += e; }
;             l = sum_x32(l); l += __builtin_amdgcn_exp2f(sink2 - mx);
;             f32x16 o[2]; o[0] = (f32x16){}; o[1] = (f32x16){};
;             const LAS unsigned char* vb = lds + VIMG + ((lane >> 4) & 1) * 32 + (lane & 3) * 8 + (4 * hi + ((lane & 15) >> 2)) * 64;
; #pragma unroll
;             for (int jt = 0; jt < 5; ++jt)
; #pragma unroll
;                 for (int s = 0; s < 2; ++s) { u32x4 w; w.x = cvt_pk_bf16(p[jt][8 * s], p[jt][8 * s + 1]); w.y = cvt_pk_bf16(p[jt][8 * s + 2], p[jt][8 * s + 3]); w.z = cvt_pk_bf16(p[jt][8 * s + 4], p[jt][8 * s + 5]); w.w = cvt_pk_bf16(p[jt][8 * s + 6], p[jt][8 * s + 7]);
;                     const bf16x8 pa = __builtin_bit_cast(bf16x8, w);
; #pragma unroll
;                     for (int d0 = 0; d0 < 2; ++d0) { const LAS unsigned char* vp = vb + d0 * 16384 + (32 * (kt0 + jt) + 16 * s) * 64; const s16x4 lo = vtr(vp), hv = vtr(vp + 8 * 64);
;                         const bf16x8 vf = (bf16x8){lo[0], lo[1], lo[2], lo[3], hv[0], hv[1], hv[2], hv[3]};
;                         o[d0] = __builtin_amdgcn_mfma_f32_32x32x16_bf16(pa, vf, o[d0], 0, 0, 0); } }
	v_add_f32_e32 v14, v14, v0
	v_add_f32_e32 v13, v15, v1
	v_max3_f32 v0, v2, v14, v13
	v_mov_b32_e32 v1, v0
	s_nop 1
	v_permlane32_swap_b32_e32 v0, v1
	v_max_f32_e32 v1, v1, v1
	v_max_f32_e32 v0, v0, v0
	v_max_f32_e32 v32, v0, v1
	v_sub_f32_e32 v0, v96, v32
	v_exp_f32_e32 v0, v0
	v_sub_f32_e32 v1, v64, v32
	v_exp_f32_e32 v1, v1
	v_sub_f32_e32 v64, v71, v32
	v_add_f32_e32 v2, 0, v0
	v_exp_f32_e32 v64, v64
	v_add_f32_e32 v3, v1, v2
	v_sub_f32_e32 v2, v66, v32
	v_exp_f32_e32 v2, v2
	v_sub_f32_e32 v48, v48, v32
	v_sub_f32_e32 v33, v33, v32
	v_sub_f32_e32 v16, v16, v32
	v_add_f32_e32 v4, v2, v3
	v_sub_f32_e32 v3, v65, v32
	v_exp_f32_e32 v3, v3
	v_sub_f32_e32 v65, v69, v32
	v_exp_f32_e32 v66, v65
	v_sub_f32_e32 v65, v73, v32
	v_add_f32_e32 v5, v3, v4
	v_sub_f32_e32 v4, v68, v32
	v_exp_f32_e32 v4, v4
	v_exp_f32_e32 v68, v65
	v_sub_f32_e32 v65, v72, v32
	v_exp_f32_e32 v72, v65
	v_add_f32_e32 v6, v4, v5
	v_sub_f32_e32 v5, v67, v32
	v_exp_f32_e32 v5, v5
	v_sub_f32_e32 v65, v75, v32
	v_exp_f32_e32 v75, v65
	v_sub_f32_e32 v65, v74, v32
	v_add_f32_e32 v7, v5, v6
	v_sub_f32_e32 v6, v97, v32
	v_exp_f32_e32 v6, v6
	v_exp_f32_e32 v97, v65
	v_sub_f32_e32 v65, v78, v32
	v_exp_f32_e32 v102, v65
	v_add_f32_e32 v15, v6, v7
	v_sub_f32_e32 v7, v70, v32
	v_exp_f32_e32 v7, v7
	v_sub_f32_e32 v65, v76, v32
	v_exp_f32_e32 v162, v65
	v_sub_f32_e32 v65, v77, v32
	v_add_f32_e32 v15, v7, v15
	v_add_f32_e32 v15, v64, v15
	v_add_f32_e32 v15, v66, v15
	v_add_f32_e32 v15, v68, v15
	v_add_f32_e32 v15, v72, v15
	v_add_f32_e32 v15, v75, v15
	v_exp_f32_e32 v65, v65
	v_add_f32_e32 v15, v97, v15
	v_exp_f32_e32 v67, v48
	v_sub_f32_e32 v48, v50, v32
	v_add_f32_e32 v15, v102, v15
	v_exp_f32_e32 v70, v48
	v_sub_f32_e32 v48, v49, v32
	v_add_f32_e32 v15, v162, v15
	v_exp_f32_e32 v76, v48
	v_sub_f32_e32 v48, v52, v32
	v_add_f32_e32 v15, v65, v15
	v_exp_f32_e32 v96, v48
	v_sub_f32_e32 v48, v51, v32
	v_add_f32_e32 v15, v67, v15
	v_exp_f32_e32 v101, v48
	v_sub_f32_e32 v48, v79, v32
	v_add_f32_e32 v15, v70, v15
	v_exp_f32_e32 v156, v48
	v_sub_f32_e32 v48, v54, v32
	v_add_f32_e32 v15, v76, v15
	v_exp_f32_e32 v166, v48
	v_sub_f32_e32 v48, v55, v32
	v_add_f32_e32 v15, v96, v15
	v_exp_f32_e32 v55, v48
	v_sub_f32_e32 v48, v53, v32
	v_add_f32_e32 v15, v101, v15
	v_exp_f32_e32 v69, v48
	v_sub_f32_e32 v48, v57, v32
	v_add_f32_e32 v15, v156, v15
	v_exp_f32_e32 v71, v48
	v_sub_f32_e32 v48, v56, v32
	v_add_f32_e32 v15, v166, v15
	v_exp_f32_e32 v79, v48
	v_sub_f32_e32 v48, v59, v32
	v_add_f32_e32 v15, v55, v15
	v_exp_f32_e32 v99, v48
	v_sub_f32_e32 v48, v58, v32
	v_add_f32_e32 v15, v69, v15
	v_exp_f32_e32 v105, v48
	v_sub_f32_e32 v48, v62, v32
	v_add_f32_e32 v15, v71, v15
	v_exp_f32_e32 v161, v48
	v_sub_f32_e32 v48, v60, v32
	v_add_f32_e32 v15, v79, v15
	v_exp_f32_e32 v168, v48
	v_sub_f32_e32 v48, v61, v32
	v_add_f32_e32 v15, v99, v15
	v_exp_f32_e32 v59, v48
	v_add_f32_e32 v15, v105, v15
	v_exp_f32_e32 v62, v33
	v_sub_f32_e32 v33, v63, v32
	v_add_f32_e32 v15, v161, v15
	v_exp_f32_e32 v74, v33
	v_sub_f32_e32 v33, v34, v32
	v_add_f32_e32 v15, v168, v15
	v_exp_f32_e32 v100, v33
	v_sub_f32_e32 v33, v36, v32
	v_add_f32_e32 v15, v59, v15
	v_exp_f32_e32 v104, v33
	v_sub_f32_e32 v33, v35, v32
	v_add_f32_e32 v15, v62, v15
	v_exp_f32_e32 v159, v33
	v_sub_f32_e32 v33, v98, v32
	v_add_f32_e32 v15, v74, v15
	v_exp_f32_e32 v165, v33
	v_sub_f32_e32 v33, v38, v32
	v_add_f32_e32 v15, v100, v15
	v_exp_f32_e32 v169, v33
	v_sub_f32_e32 v33, v39, v32
	v_add_f32_e32 v15, v104, v15
	v_exp_f32_e32 v61, v33
	v_sub_f32_e32 v33, v37, v32
	v_add_f32_e32 v15, v159, v15
	v_exp_f32_e32 v73, v33
	v_sub_f32_e32 v33, v41, v32
	v_add_f32_e32 v15, v165, v15
	v_exp_f32_e32 v78, v33
	v_sub_f32_e32 v33, v40, v32
	v_add_f32_e32 v15, v169, v15
	v_exp_f32_e32 v103, v33
	v_sub_f32_e32 v33, v43, v32
	v_add_f32_e32 v15, v61, v15
	v_exp_f32_e32 v157, v33
	v_sub_f32_e32 v33, v42, v32
	v_add_f32_e32 v15, v73, v15
	v_exp_f32_e32 v164, v33
	v_sub_f32_e32 v33, v46, v32
	v_add_f32_e32 v15, v78, v15
	v_exp_f32_e32 v167, v33
	v_sub_f32_e32 v33, v44, v32
	v_add_f32_e32 v15, v103, v15
	v_exp_f32_e32 v170, v33
	v_sub_f32_e32 v33, v45, v32
	v_add_f32_e32 v15, v157, v15
	v_exp_f32_e32 v63, v33
	v_add_f32_e32 v15, v164, v15
	v_exp_f32_e32 v77, v16
	v_sub_f32_e32 v16, v18, v32
	v_add_f32_e32 v15, v167, v15
	v_exp_f32_e32 v98, v16
	v_sub_f32_e32 v16, v17, v32
	v_add_f32_e32 v15, v170, v15
	v_exp_f32_e32 v106, v16
	v_sub_f32_e32 v16, v20, v32
	v_add_f32_e32 v15, v63, v15
	v_exp_f32_e32 v107, v16
	v_sub_f32_e32 v16, v19, v32
	v_add_f32_e32 v15, v77, v15
	v_exp_f32_e32 v158, v16
	v_sub_f32_e32 v16, v22, v32
	v_add_f32_e32 v15, v98, v15
	v_exp_f32_e32 v160, v16
	v_sub_f32_e32 v16, v21, v32
	v_add_f32_e32 v15, v106, v15
	v_exp_f32_e32 v163, v16
	v_sub_f32_e32 v16, v24, v32
	v_add_f32_e32 v15, v107, v15
	v_exp_f32_e32 v51, v16
	v_sub_f32_e32 v16, v23, v32
	v_add_f32_e32 v15, v158, v15
	v_exp_f32_e32 v52, v16
	v_sub_f32_e32 v16, v26, v32
	v_add_f32_e32 v15, v160, v15
	v_exp_f32_e32 v53, v16
	v_sub_f32_e32 v16, v25, v32
	v_add_f32_e32 v15, v163, v15
	v_exp_f32_e32 v54, v16
	v_sub_f32_e32 v16, v28, v32
	v_add_f32_e32 v15, v51, v15
	v_exp_f32_e32 v56, v16
	v_sub_f32_e32 v16, v27, v32
	v_add_f32_e32 v15, v52, v15
	v_exp_f32_e32 v57, v16
	v_sub_f32_e32 v16, v30, v32
	v_add_f32_e32 v15, v53, v15
	v_exp_f32_e32 v58, v16
	v_sub_f32_e32 v16, v29, v32
	v_add_f32_e32 v15, v54, v15
	v_exp_f32_e32 v60, v16
	v_sub_f32_e32 v16, v47, v32
	v_add_f32_e32 v15, v56, v15
	v_exp_f32_e32 v43, v16
	v_sub_f32_e32 v16, v31, v32
	v_add_f32_e32 v15, v57, v15
	v_exp_f32_e32 v44, v16
	v_sub_f32_e32 v16, v172, v32
	v_add_f32_e32 v15, v58, v15
	v_exp_f32_e32 v45, v16
	v_sub_f32_e32 v16, v171, v32
	v_add_f32_e32 v15, v60, v15
	v_exp_f32_e32 v46, v16
	v_sub_f32_e32 v16, v174, v32
	v_add_f32_e32 v15, v43, v15
	v_exp_f32_e32 v47, v16
	v_sub_f32_e32 v16, v173, v32
	v_add_f32_e32 v15, v44, v15
	v_exp_f32_e32 v48, v16
	v_sub_f32_e32 v16, v176, v32
	v_add_f32_e32 v15, v45, v15
	v_exp_f32_e32 v49, v16
	v_sub_f32_e32 v16, v175, v32
	v_add_f32_e32 v15, v46, v15
	v_exp_f32_e32 v50, v16
	v_sub_f32_e32 v16, v177, v32
	v_add_f32_e32 v15, v47, v15
	v_exp_f32_e32 v35, v16
	v_sub_f32_e32 v8, v8, v32
	v_add_f32_e32 v15, v48, v15
	v_exp_f32_e32 v36, v8
	v_sub_f32_e32 v10, v10, v32
	v_add_f32_e32 v15, v49, v15
	v_exp_f32_e32 v37, v10
	v_sub_f32_e32 v9, v9, v32
	v_add_f32_e32 v15, v50, v15
	v_exp_f32_e32 v38, v9
	v_sub_f32_e32 v9, v12, v32
	v_add_f32_e32 v15, v35, v15
	v_exp_f32_e32 v39, v9
	v_sub_f32_e32 v9, v11, v32
	v_add_f32_e32 v8, v36, v15
	v_exp_f32_e32 v40, v9
	v_sub_f32_e32 v9, v14, v32
	v_add_u32_e32 v171, s82, v125
	v_add_f32_e32 v8, v37, v8
	v_exp_f32_e32 v41, v9
	v_sub_f32_e32 v9, v13, v32
	v_cvt_pk_bf16_f32 v16, v0, v1
	v_cvt_pk_bf16_f32 v17, v2, v3
	v_cvt_pk_bf16_f32 v18, v4, v5
	v_cvt_pk_bf16_f32 v19, v6, v7
	ds_read_b64_tr_b16 v[0:1], v171 offset:32768
	ds_read_b64_tr_b16 v[2:3], v171 offset:33280
	v_add_f32_e32 v8, v38, v8
	v_exp_f32_e32 v42, v9
	v_add_f32_e32 v8, v39, v8
	v_add_f32_e32 v8, v40, v8
	v_add_f32_e32 v8, v41, v8
	v_add_f32_e32 v33, v42, v8
	s_waitcnt lgkmcnt(0)
; #define LAS __attribute__((address_space(3)))
; __device__ __forceinline__ float sum_x32(float v) { const unsigned u = __builtin_bit_cast(unsigned, v); auto rr = __builtin_amdgcn_permlane32_swap(u, u, false, false); return __builtin_bit_cast(float, (unsigned)rr[0]) + __builtin_bit_cast(float, (unsigned)rr[1]); }
; __device__ __forceinline__ unsigned cvt_pk_bf16(float lo, float hi) { unsigned r; asm volatile("v_cvt_pk_bf16_f32 %0, %1, %2" : "=v"(r) : "v"(lo), "v"(hi)); return r; }
; __device__ __forceinline__ s16x4 vtr(const LAS unsigned char* p) { return __builtin_bit_cast(s16x4, __builtin_amdgcn_ds_read_tr16_b64_v4i16((LAS s16x4*)p)); }
; __device__ __forceinline__ void attn_phase(LAS unsigned char* lds, const bf16* U, bf16* YA, const float* sinks, const float* rel_bias, int G, int c, int wbase, int y8) {
;     ...
;             l = sum_x32(l); l += __builtin_amdgcn_exp2f(sink2 - mx);
;             f32x16 o[2]; o[0] = (f32x16){}; o[1] = (f32x16){};
;             const LAS unsigned char* vb = lds + VIMG + ((lane >> 4) & 1) * 32 + (lane & 3) * 8 + (4 * hi + ((lane & 15) >> 2)) * 64;
; #pragma unroll
;             for (int jt = 0; jt < 5; ++jt)
; #pragma unroll
;                 for (int s = 0; s < 2; ++s) { u32x4 w; w.x = cvt_pk_bf16(p[jt][8 * s], p[jt][8 * s + 1]); w.y = cvt_pk_bf16(p[jt][8 * s + 2], p[jt][8 * s + 3]); w.z = cvt_pk_bf16(p[jt][8 * s + 4], p[jt][8 * s + 5]); w.w = cvt_pk_bf16(p[jt][8 * s + 6], p[jt][8 * s + 7]);
;                     const bf16x8 pa = __builtin_bit_cast(bf16x8, w);
; #pragma unroll
;                     for (int d0 = 0; d0 < 2; ++d0) { const LAS unsigned char* vp = vb + d0 * 16384 + (32 * (kt0 + jt) + 16 * s) * 64; const s16x4 lo = vtr(vp), hv = vtr(vp + 8 * 64);
;                         const bf16x8 vf = (bf16x8){lo[0], lo[1], lo[2], lo[3], hv[0], hv[1], hv[2], hv[3]};
;                         o[d0] = __builtin_amdgcn_mfma_f32_32x32x16_bf16(pa, vf, o[d0], 0, 0, 0); } }
;             if (hi == 0) lscr[r32] = l;
	v_mfma_f32_32x32x16_bf16 v[0:15], v[16:19], v[0:3], 0
	ds_read_b64_tr_b16 v[20:21], v171 offset:49152
	ds_read_b64_tr_b16 v[22:23], v171 offset:49664
	v_cvt_pk_bf16_f32 v172, v64, v66
	v_cvt_pk_bf16_f32 v173, v68, v72
	v_cvt_pk_bf16_f32 v174, v75, v97
	v_cvt_pk_bf16_f32 v175, v102, v162
	ds_read_b64_tr_b16 v[176:177], v171 offset:33792
	ds_read_b64_tr_b16 v[178:179], v171 offset:34304
	v_add_u32_e32 v102, s12, v125
	s_waitcnt lgkmcnt(2)
	v_mfma_f32_32x32x16_bf16 v[16:31], v[16:19], v[20:23], 0
	v_mov_b32_e32 v34, v33
	s_nop 1
	v_permlane32_swap_b32_e32 v33, v34
	s_waitcnt lgkmcnt(0)
	v_mfma_f32_32x32x16_bf16 v[0:15], v[172:175], v[176:179], v[0:15]
	ds_read_b64_tr_b16 v[176:177], v171 offset:50176
	ds_read_b64_tr_b16 v[178:179], v171 offset:50688
	v_cvt_pk_bf16_f32 v64, v65, v67
	v_cvt_pk_bf16_f32 v65, v70, v76
	v_cvt_pk_bf16_f32 v66, v96, v101
	v_add_u32_e32 v101, s83, v125
	v_cvt_pk_bf16_f32 v67, v156, v166
	s_waitcnt lgkmcnt(0)
	v_mfma_f32_32x32x16_bf16 v[16:31], v[172:175], v[176:179], v[16:31]
	ds_read_b64_tr_b16 v[172:173], v101 offset:32768
	ds_read_b64_tr_b16 v[174:175], v101 offset:33280
	s_waitcnt lgkmcnt(0)
	v_mfma_f32_32x32x16_bf16 v[0:15], v[64:67], v[172:175], v[0:15]
	ds_read_b64_tr_b16 v[172:173], v101 offset:49152
	ds_read_b64_tr_b16 v[174:175], v101 offset:49664
	s_waitcnt lgkmcnt(0)
	v_mfma_f32_32x32x16_bf16 v[16:31], v[64:67], v[172:175], v[16:31]
	v_cvt_pk_bf16_f32 v64, v55, v69
	v_cvt_pk_bf16_f32 v65, v71, v79
	v_cvt_pk_bf16_f32 v66, v99, v105
	v_cvt_pk_bf16_f32 v67, v161, v168
	ds_read_b64_tr_b16 v[68:69], v101 offset:33792
	ds_read_b64_tr_b16 v[70:71], v101 offset:34304
	s_waitcnt lgkmcnt(0)
	v_mfma_f32_32x32x16_bf16 v[0:15], v[64:67], v[68:71], v[0:15]
	ds_read_b64_tr_b16 v[68:69], v101 offset:50176
	ds_read_b64_tr_b16 v[70:71], v101 offset:50688
	s_waitcnt lgkmcnt(0)
	v_mfma_f32_32x32x16_bf16 v[16:31], v[64:67], v[68:71], v[16:31]
	v_cvt_pk_bf16_f32 v64, v59, v62
	v_cvt_pk_bf16_f32 v65, v74, v100
	v_cvt_pk_bf16_f32 v66, v104, v159
	v_cvt_pk_bf16_f32 v67, v165, v169
	ds_read_b64_tr_b16 v[68:69], v102 offset:32768
	ds_read_b64_tr_b16 v[70:71], v102 offset:33280
	v_add_u32_e32 v104, s56, v125
	s_waitcnt lgkmcnt(0)
	v_mfma_f32_32x32x16_bf16 v[0:15], v[64:67], v[68:71], v[0:15]
	ds_read_b64_tr_b16 v[68:69], v102 offset:49152
	ds_read_b64_tr_b16 v[70:71], v102 offset:49664
	s_waitcnt lgkmcnt(0)
	v_mfma_f32_32x32x16_bf16 v[16:31], v[64:67], v[68:71], v[16:31]
	v_cvt_pk_bf16_f32 v64, v61, v73
	v_cvt_pk_bf16_f32 v65, v78, v103
	v_cvt_pk_bf16_f32 v66, v157, v164
	v_cvt_pk_bf16_f32 v67, v167, v170
	ds_read_b64_tr_b16 v[68:69], v102 offset:33792
	ds_read_b64_tr_b16 v[70:71], v102 offset:34304
	v_add_u32_e32 v103, s13, v125
	s_waitcnt lgkmcnt(0)
	v_mfma_f32_32x32x16_bf16 v[0:15], v[64:67], v[68:71], v[0:15]
	ds_read_b64_tr_b16 v[68:69], v102 offset:50176
	ds_read_b64_tr_b16 v[70:71], v102 offset:50688
	v_cvt_pk_bf16_f32 v62, v63, v77
	v_cvt_pk_bf16_f32 v63, v98, v106
	s_waitcnt lgkmcnt(0)
	v_mfma_f32_32x32x16_bf16 v[16:31], v[64:67], v[68:71], v[16:31]
	v_cvt_pk_bf16_f32 v64, v107, v158
	v_cvt_pk_bf16_f32 v65, v160, v163
	ds_read_b64_tr_b16 v[66:67], v103 offset:32768
	ds_read_b64_tr_b16 v[68:69], v103 offset:33280
	s_waitcnt lgkmcnt(0)
	v_mfma_f32_32x32x16_bf16 v[0:15], v[62:65], v[66:69], v[0:15]
	ds_read_b64_tr_b16 v[66:67], v103 offset:49152
	ds_read_b64_tr_b16 v[68:69], v103 offset:49664
	v_cvt_pk_bf16_f32 v52, v51, v52
	v_cvt_pk_bf16_f32 v53, v53, v54
	v_cvt_pk_bf16_f32 v54, v56, v57
	v_cvt_pk_bf16_f32 v55, v58, v60
	ds_read_b64_tr_b16 v[56:57], v103 offset:33792
	ds_read_b64_tr_b16 v[58:59], v103 offset:34304
	s_waitcnt lgkmcnt(2)
	v_mfma_f32_32x32x16_bf16 v[16:31], v[62:65], v[66:69], v[16:31]
	s_waitcnt lgkmcnt(0)
	v_mfma_f32_32x32x16_bf16 v[0:15], v[52:55], v[56:59], v[0:15]
	ds_read_b64_tr_b16 v[56:57], v103 offset:50176
	ds_read_b64_tr_b16 v[58:59], v103 offset:50688
	v_cvt_pk_bf16_f32 v44, v43, v44
	v_cvt_pk_bf16_f32 v45, v45, v46
	v_cvt_pk_bf16_f32 v46, v47, v48
	v_cvt_pk_bf16_f32 v47, v49, v50
	ds_read_b64_tr_b16 v[48:49], v104 offset:32768
	ds_read_b64_tr_b16 v[50:51], v104 offset:33280
	s_waitcnt lgkmcnt(2)
	v_mfma_f32_32x32x16_bf16 v[16:31], v[52:55], v[56:59], v[16:31]
	s_waitcnt lgkmcnt(0)
	v_mfma_f32_32x32x16_bf16 v[0:15], v[44:47], v[48:51], v[0:15]
	ds_read_b64_tr_b16 v[48:49], v104 offset:49152
	ds_read_b64_tr_b16 v[50:51], v104 offset:49664
	v_cvt_pk_bf16_f32 v36, v35, v36
	v_cvt_pk_bf16_f32 v37, v37, v38
	v_cvt_pk_bf16_f32 v38, v39, v40
	v_cvt_pk_bf16_f32 v39, v41, v42
	ds_read_b64_tr_b16 v[40:41], v104 offset:33792
	ds_read_b64_tr_b16 v[42:43], v104 offset:34304
	s_waitcnt lgkmcnt(2)
	v_mfma_f32_32x32x16_bf16 v[16:31], v[44:47], v[48:51], v[16:31]
	s_waitcnt lgkmcnt(0)
	v_mfma_f32_32x32x16_bf16 v[0:15], v[36:39], v[40:43], v[0:15]
	ds_read_b64_tr_b16 v[40:41], v104 offset:50176
	ds_read_b64_tr_b16 v[42:43], v104 offset:50688
	s_waitcnt lgkmcnt(0)
	v_mfma_f32_32x32x16_bf16 v[16:31], v[36:39], v[40:43], v[16:31]
	s_and_saveexec_b64 s[30:31], s[2:3]
	s_cbranch_execz .LBB0_556
	v_sub_f32_e32 v32, v151, v32
	v_exp_f32_e32 v32, v32
	v_add_f32_e32 v33, v33, v34
	v_add_f32_e32 v32, v33, v32
	ds_write_b32 v126, v32
